# R3 attention loop plus workgroup-uniform fast-or-slow softmax path decision via an LDS flag; the previous measurement v041 was mislabeled (it was a timing probe that ran the mLSTM output phase twice)
# speedup vs baseline: 1.0001x; 1.0001x over previous
.LBB0_1127:
	s_lshl_b32 s0, s2, 3
	s_or_b32 s0, s0, s35
	v_lshl_add_u32 v5, s0, 6, v203
	v_lshl_add_u32 v4, v190, 1, v10
	v_mad_u64_u32 v[204:205], s[12:13], v5, s28, v[192:193]
	s_waitcnt vmcnt(0)
	v_and_b32_e32 v5, 0xffff0000, v132
	v_subrev_u32_e32 v202, s44, v4
	v_lshlrev_b32_e32 v4, 16, v132
	v_mul_f32_e32 v6, v5, v5
	v_fmac_f32_e32 v6, v4, v4
	v_lshlrev_b32_e32 v4, 16, v133
	v_fmac_f32_e32 v6, v4, v4
	v_and_b32_e32 v4, 0xffff0000, v133
	v_fmac_f32_e32 v6, v4, v4
	v_lshlrev_b32_e32 v4, 16, v134
	v_fmac_f32_e32 v6, v4, v4
	v_and_b32_e32 v4, 0xffff0000, v134
	v_fmac_f32_e32 v6, v4, v4
	v_lshlrev_b32_e32 v4, 16, v135
	v_fmac_f32_e32 v6, v4, v4
	v_and_b32_e32 v4, 0xffff0000, v135
	v_fmac_f32_e32 v6, v4, v4
	v_lshlrev_b32_e32 v4, 16, v136
	v_fmac_f32_e32 v6, v4, v4
	v_and_b32_e32 v4, 0xffff0000, v136
	v_fmac_f32_e32 v6, v4, v4
	v_lshlrev_b32_e32 v4, 16, v137
	v_fmac_f32_e32 v6, v4, v4
	v_and_b32_e32 v4, 0xffff0000, v137
	v_fmac_f32_e32 v6, v4, v4
	v_lshlrev_b32_e32 v4, 16, v138
	v_fmac_f32_e32 v6, v4, v4
	v_and_b32_e32 v4, 0xffff0000, v138
	v_fmac_f32_e32 v6, v4, v4
	v_lshlrev_b32_e32 v4, 16, v139
	v_fmac_f32_e32 v6, v4, v4
	v_and_b32_e32 v4, 0xffff0000, v139
	v_fmac_f32_e32 v6, v4, v4
	v_lshlrev_b32_e32 v4, 16, v140
	v_fmac_f32_e32 v6, v4, v4
	v_and_b32_e32 v4, 0xffff0000, v140
	v_fmac_f32_e32 v6, v4, v4
	v_lshlrev_b32_e32 v4, 16, v141
	v_fmac_f32_e32 v6, v4, v4
	v_and_b32_e32 v4, 0xffff0000, v141
	v_fmac_f32_e32 v6, v4, v4
	v_lshlrev_b32_e32 v4, 16, v142
	v_fmac_f32_e32 v6, v4, v4
	v_and_b32_e32 v4, 0xffff0000, v142
	v_fmac_f32_e32 v6, v4, v4
	v_lshlrev_b32_e32 v4, 16, v143
	v_fmac_f32_e32 v6, v4, v4
	v_and_b32_e32 v4, 0xffff0000, v143
	v_fmac_f32_e32 v6, v4, v4
	v_lshlrev_b32_e32 v4, 16, v144
	v_fmac_f32_e32 v6, v4, v4
	v_and_b32_e32 v4, 0xffff0000, v144
	v_fmac_f32_e32 v6, v4, v4
	v_lshlrev_b32_e32 v4, 16, v145
	v_fmac_f32_e32 v6, v4, v4
	v_and_b32_e32 v4, 0xffff0000, v145
	v_fmac_f32_e32 v6, v4, v4
	v_lshlrev_b32_e32 v4, 16, v146
	v_fmac_f32_e32 v6, v4, v4
	v_and_b32_e32 v4, 0xffff0000, v146
	v_fmac_f32_e32 v6, v4, v4
	v_lshlrev_b32_e32 v4, 16, v147
	v_fmac_f32_e32 v6, v4, v4
	v_and_b32_e32 v4, 0xffff0000, v147
	v_fmac_f32_e32 v6, v4, v4
	v_lshlrev_b32_e32 v4, 16, v148
	v_fmac_f32_e32 v6, v4, v4
	v_and_b32_e32 v4, 0xffff0000, v148
	v_fmac_f32_e32 v6, v4, v4
	v_lshlrev_b32_e32 v4, 16, v149
	v_fmac_f32_e32 v6, v4, v4
	v_and_b32_e32 v4, 0xffff0000, v149
	v_fmac_f32_e32 v6, v4, v4
	v_lshlrev_b32_e32 v4, 16, v150
	v_fmac_f32_e32 v6, v4, v4
	v_and_b32_e32 v4, 0xffff0000, v150
	v_fmac_f32_e32 v6, v4, v4
	v_lshlrev_b32_e32 v4, 16, v151
	v_fmac_f32_e32 v6, v4, v4
	v_and_b32_e32 v4, 0xffff0000, v151
	v_fmac_f32_e32 v6, v4, v4
	v_and_b32_e32 v5, 0xffff0000, v152
	v_lshlrev_b32_e32 v4, 16, v152
	v_pk_mul_f32 v[4:5], v[4:5], v[4:5]
	s_ashr_i32 s1, s0, 31
	v_add_f32_e32 v4, v4, v6
	v_add_f32_e32 v6, v5, v4
	v_and_b32_e32 v5, 0xffff0000, v153
	v_lshlrev_b32_e32 v4, 16, v153
	v_pk_mul_f32 v[4:5], v[4:5], v[4:5]
	s_lshl_b64 s[0:1], s[0:1], 2
	v_add_f32_e32 v4, v4, v6
	v_add_f32_e32 v6, v5, v4
	v_and_b32_e32 v5, 0xffff0000, v154
	v_lshlrev_b32_e32 v4, 16, v154
	v_pk_mul_f32 v[4:5], v[4:5], v[4:5]
	s_add_u32 s0, s21, s0
	v_add_f32_e32 v4, v4, v6
	v_add_f32_e32 v6, v5, v4
	v_and_b32_e32 v5, 0xffff0000, v155
	v_lshlrev_b32_e32 v4, 16, v155
	v_pk_mul_f32 v[4:5], v[4:5], v[4:5]
	s_addc_u32 s1, s22, s1
	v_add_f32_e32 v4, v4, v6
	s_ashr_i32 s3, s2, 31
	v_add_f32_e32 v4, v5, v4
	global_load_dword v5, v3, s[0:1]
	s_lshl_b64 s[0:1], s[2:3], 2
	s_add_u32 s0, s21, s0
	s_addc_u32 s1, s22, s1
	global_load_dword v7, v3, s[0:1] offset:256
	v_mov_b32_e32 v6, v4
	s_nop 1
	v_permlane32_swap_b32_e32 v4, v6
	s_mov_b32 s0, 0x45fd2000
	v_subrev_u32_e32 v223, s44, v8
	s_barrier
	v_mad_i32_i24 v8, v199, s23, v202
	v_add_u32_e32 v205, v216, v217
	s_mov_b64 s[2:3], exec
	global_load_dwordx2 v[16:17], v8, s[44:45]
	v_lshl_add_u32 v8, s23, 7, v204
	global_load_dwordx4 v[8:11], v8, s[44:45]
	s_waitcnt vmcnt(2)
	v_pk_add_f32 v[4:5], v[4:5], v[6:7]
	s_nop 0
	v_mul_f32_e32 v4, v4, v5
	v_cmp_gt_f32_e32 vcc, s0, v4
	s_nop 1
	s_cmp_eq_u64 vcc, s[2:3]
	s_cbranch_scc1 .Latt_flag_skip
	s_add_i32 s12, s15, 1
	v_mov_b32_e32 v178, 0x27f80
	v_mov_b32_e32 v179, s12
	ds_write_b32 v178, v179
.Latt_flag_skip:
	s_or_b32 s0, s23, 1
	s_sub_i32 s1, s0, s34
	v_lshl_add_u32 v4, s23, v215, v223
	s_min_u32 s0, s0, s1
	global_load_dwordx4 v[4:7], v4, s[44:45]
	v_lshl_add_u32 v12, s0, v215, v223
	global_load_dwordx4 v[12:15], v12, s[44:45]
	v_mad_i32_i24 v18, v199, s0, v202
	global_load_dwordx2 v[18:19], v18, s[44:45]
	s_waitcnt vmcnt(2)
	ds_write_b128 v219, v[4:7]
	ds_write_b64 v220, v[16:17]
	s_waitcnt vmcnt(1)
	ds_write_b128 v219, v[12:15] offset:13312
	s_waitcnt vmcnt(0)
	ds_write_b64 v220, v[18:19] offset:13312
	ds_write_b64 v221, v[8:9] offset:26624
	ds_write_b64 v222, v[10:11] offset:26624
	s_waitcnt lgkmcnt(0)
	s_barrier
	ds_read_b128 v[4:7], v205 offset:6656
	ds_read_b128 v[8:11], v205
	ds_read_b128 v[36:39], v205 offset:32
	ds_read_b128 v[40:43], v205 offset:6688
	s_waitcnt lgkmcnt(2)
	v_mfma_f32_32x32x16_bf16 v[20:35], v[8:11], v[132:135], 0
	v_mfma_f32_32x32x16_bf16 v[4:19], v[4:7], v[132:135], 0
	s_waitcnt lgkmcnt(1)
	v_mfma_f32_32x32x16_bf16 v[20:35], v[36:39], v[136:139], v[20:35]
	s_waitcnt lgkmcnt(0)
	v_mfma_f32_32x32x16_bf16 v[4:19], v[40:43], v[136:139], v[4:19]
	ds_read_b128 v[36:39], v205 offset:64
	ds_read_b128 v[40:43], v205 offset:6720
	s_waitcnt lgkmcnt(1)
	v_mfma_f32_32x32x16_bf16 v[20:35], v[36:39], v[140:143], v[20:35]
	s_waitcnt lgkmcnt(0)
	v_mfma_f32_32x32x16_bf16 v[4:19], v[40:43], v[140:143], v[4:19]
	ds_read_b128 v[36:39], v205 offset:96
	ds_read_b128 v[40:43], v205 offset:6752
	s_waitcnt lgkmcnt(1)
	v_mfma_f32_32x32x16_bf16 v[20:35], v[36:39], v[144:147], v[20:35]
	s_waitcnt lgkmcnt(0)
	v_mfma_f32_32x32x16_bf16 v[4:19], v[40:43], v[144:147], v[4:19]
	ds_read_b128 v[36:39], v205 offset:128
	ds_read_b128 v[40:43], v205 offset:6784
	s_waitcnt lgkmcnt(1)
	v_mfma_f32_32x32x16_bf16 v[20:35], v[36:39], v[148:151], v[20:35]
	s_waitcnt lgkmcnt(0)
	v_mfma_f32_32x32x16_bf16 v[4:19], v[40:43], v[148:151], v[4:19]
	ds_read_b128 v[36:39], v205 offset:160
	ds_read_b128 v[40:43], v205 offset:6816
	s_waitcnt lgkmcnt(0)
	s_barrier
	v_mfma_f32_32x32x16_bf16 v[20:35], v[36:39], v[152:155], v[20:35]
	v_mfma_f32_32x32x16_bf16 v[4:19], v[40:43], v[152:155], v[4:19]
	v_mov_b32_e32 v178, 0x27f80
	ds_read_b32 v179, v178
	s_add_i32 s12, s15, 1
	s_waitcnt lgkmcnt(0)
	v_cmp_ne_u32_e64 s[0:1], s12, v179
	s_nop 1
	s_and_b64 vcc, vcc, s[0:1]
	s_and_saveexec_b64 s[0:1], s[42:43]
	s_setprio 1
	s_or_b64 exec, exec, s[0:1]
	s_cmp_eq_u64 vcc, s[2:3]
	s_mov_b64 s[0:1], -1
	s_cbranch_scc1 .LBB0_1136
	v_mov_b32_e32 v50, v3
	v_mov_b32_e32 v51, v3
	v_mov_b32_e32 v36, v3
	v_mov_b32_e32 v37, v3
	v_mov_b32_e32 v38, v3
	v_mov_b32_e32 v39, v3
	v_mov_b32_e32 v40, v3
	v_mov_b32_e32 v41, v3
	v_mov_b32_e32 v42, v3
	v_mov_b32_e32 v43, v3
	v_mov_b32_e32 v44, v3
	v_mov_b32_e32 v45, v3
	v_mov_b32_e32 v46, v3
	v_mov_b32_e32 v47, v3
	v_mov_b32_e32 v48, v3
	v_mov_b32_e32 v49, v3
	v_mov_b64_e32 v[66:67], v[50:51]
	v_mov_b64_e32 v[82:83], v[34:35]
	v_mov_b64_e32 v[98:99], v[18:19]
	s_mov_b32 s0, 0
	v_mov_b32_e32 v224, 0
	v_mov_b32_e32 v225, 0xf149f2ca
	v_mov_b64_e32 v[64:65], v[48:49]
	v_mov_b64_e32 v[62:63], v[46:47]
	v_mov_b64_e32 v[60:61], v[44:45]
	v_mov_b64_e32 v[58:59], v[42:43]
	v_mov_b64_e32 v[56:57], v[40:41]
	v_mov_b64_e32 v[54:55], v[38:39]
	v_mov_b64_e32 v[52:53], v[36:37]
	v_mov_b64_e32 v[80:81], v[32:33]
	v_mov_b64_e32 v[78:79], v[30:31]
	v_mov_b64_e32 v[76:77], v[28:29]
	v_mov_b64_e32 v[74:75], v[26:27]
	v_mov_b64_e32 v[72:73], v[24:25]
	v_mov_b64_e32 v[70:71], v[22:23]
	v_mov_b64_e32 v[68:69], v[20:21]
	v_mov_b64_e32 v[96:97], v[16:17]
	v_mov_b64_e32 v[94:95], v[14:15]
	v_mov_b64_e32 v[92:93], v[12:13]
	v_mov_b64_e32 v[90:91], v[10:11]
	v_mov_b64_e32 v[88:89], v[8:9]
	v_mov_b64_e32 v[86:87], v[6:7]
	v_mov_b64_e32 v[84:85], v[4:5]
	s_branch .LBB0_1132
